# speedup vs baseline: 1.0101x; 1.0101x over previous
.Lpre_not160:
	s_cmpk_lt_u32 s2, 0xad
	s_cbranch_scc1 .Lpre_roleD
	s_branch .Lpre_roleE

.Lpre_roleA_new:
	s_load_dwordx4 s[4:7], s[0:1], 0x0
	s_load_dwordx2 s[8:9], s[0:1], 0x18
	s_load_dwordx2 s[10:11], s[0:1], 0x58
	s_lshr_b32 s3, s2, 3
	s_and_b32 s12, s2, 7
	v_and_b32_e32 v1, 15, v0
	v_lshrrev_b32_e32 v2, 4, v0
	v_lshlrev_b32_e32 v3, 5, v0
	v_lshlrev_b32_e32 v4, 13, v2
	v_lshl_or_b32 v4, v1, 2, v4
	v_add_u32_e32 v5, 0x1000, v4
	v_and_b32_e32 v6, 7, v2
	v_lshlrev_b32_e32 v6, 2, v6
	v_and_b32_e32 v7, 7, v0
	v_lshlrev_b32_e32 v7, 2, v7
	s_lshl_b32 s13, s3, 13
	s_lshl_b32 s14, s12, 6
	s_lshl_b32 s15, s3, 5
	s_waitcnt lgkmcnt(0)
	s_add_u32 s16, s4, s13
	s_addc_u32 s17, s5, 0
	s_add_u32 s18, s6, s14
	s_addc_u32 s19, s7, 0
	s_add_u32 s20, s8, s15
	s_addc_u32 s21, s9, 0
	global_load_dwordx4 v[8:11], v3, s[16:17]
	global_load_dwordx4 v[12:15], v3, s[16:17] offset:16
	global_load_dword v16, v4, s[18:19]
	global_load_dword v17, v4, s[18:19] offset:512
	global_load_dword v18, v4, s[18:19] offset:1024
	global_load_dword v19, v4, s[18:19] offset:1536
	global_load_dword v20, v4, s[18:19] offset:2048
	global_load_dword v21, v4, s[18:19] offset:2560
	global_load_dword v22, v4, s[18:19] offset:3072
	global_load_dword v23, v4, s[18:19] offset:3584
	global_load_dword v24, v5, s[18:19]
	global_load_dword v25, v5, s[18:19] offset:512
	global_load_dword v26, v5, s[18:19] offset:1024
	global_load_dword v27, v5, s[18:19] offset:1536
	global_load_dword v28, v5, s[18:19] offset:2048
	global_load_dword v29, v5, s[18:19] offset:2560
	global_load_dword v30, v5, s[18:19] offset:3072
	global_load_dword v31, v5, s[18:19] offset:3584
	global_load_dword v72, v6, s[20:21]
	global_load_dword v73, v7, s[20:21]
	s_waitcnt vmcnt(18)
	ds_write_b128 v3, v[8:11]
	ds_write_b128 v3, v[12:15] offset:16
	v_lshlrev_b32_e32 v74, 6, v2
	v_lshlrev_b32_e32 v75, 9, v2
	v_lshl_or_b32 v75, v1, 2, v75
	s_waitcnt lgkmcnt(0)
	s_barrier
	ds_read_b128 v[32:35], v74 offset:0
	ds_read_b128 v[36:39], v74 offset:16
	ds_read_b128 v[40:43], v74 offset:32
	ds_read_b128 v[44:47], v74 offset:48
	s_waitcnt vmcnt(2)
	ds_read_b128 v[48:51], v74 offset:1024
	ds_read_b128 v[52:55], v74 offset:1040
	ds_read_b128 v[56:59], v74 offset:1056
	ds_read_b128 v[60:63], v74 offset:1072
	s_waitcnt lgkmcnt(4)
	v_mul_f32_e32 v64, v32, v16
	v_fmac_f32_e32 v64, v33, v17
	v_fmac_f32_e32 v64, v34, v18
	v_fmac_f32_e32 v64, v35, v19
	v_fmac_f32_e32 v64, v36, v20
	v_fmac_f32_e32 v64, v37, v21
	v_fmac_f32_e32 v64, v38, v22
	v_fmac_f32_e32 v64, v39, v23
	v_fmac_f32_e32 v64, v40, v24
	v_fmac_f32_e32 v64, v41, v25
	v_fmac_f32_e32 v64, v42, v26
	v_fmac_f32_e32 v64, v43, v27
	v_fmac_f32_e32 v64, v44, v28
	v_fmac_f32_e32 v64, v45, v29
	v_fmac_f32_e32 v64, v46, v30
	v_fmac_f32_e32 v64, v47, v31
	ds_read_b128 v[32:35], v74 offset:2048
	ds_read_b128 v[36:39], v74 offset:2064
	ds_read_b128 v[40:43], v74 offset:2080
	ds_read_b128 v[44:47], v74 offset:2096
	s_waitcnt lgkmcnt(4)
	v_mul_f32_e32 v65, v48, v16
	v_fmac_f32_e32 v65, v49, v17
	v_fmac_f32_e32 v65, v50, v18
	v_fmac_f32_e32 v65, v51, v19
	v_fmac_f32_e32 v65, v52, v20
	v_fmac_f32_e32 v65, v53, v21
	v_fmac_f32_e32 v65, v54, v22
	v_fmac_f32_e32 v65, v55, v23
	v_fmac_f32_e32 v65, v56, v24
	v_fmac_f32_e32 v65, v57, v25
	v_fmac_f32_e32 v65, v58, v26
	v_fmac_f32_e32 v65, v59, v27
	v_fmac_f32_e32 v65, v60, v28
	v_fmac_f32_e32 v65, v61, v29
	v_fmac_f32_e32 v65, v62, v30
	v_fmac_f32_e32 v65, v63, v31
	ds_read_b128 v[48:51], v74 offset:3072
	ds_read_b128 v[52:55], v74 offset:3088
	ds_read_b128 v[56:59], v74 offset:3104
	ds_read_b128 v[60:63], v74 offset:3120
	s_waitcnt lgkmcnt(4)
	v_mul_f32_e32 v66, v32, v16
	v_fmac_f32_e32 v66, v33, v17
	v_fmac_f32_e32 v66, v34, v18
	v_fmac_f32_e32 v66, v35, v19
	v_fmac_f32_e32 v66, v36, v20
	v_fmac_f32_e32 v66, v37, v21
	v_fmac_f32_e32 v66, v38, v22
	v_fmac_f32_e32 v66, v39, v23
	v_fmac_f32_e32 v66, v40, v24
	v_fmac_f32_e32 v66, v41, v25
	v_fmac_f32_e32 v66, v42, v26
	v_fmac_f32_e32 v66, v43, v27
	v_fmac_f32_e32 v66, v44, v28
	v_fmac_f32_e32 v66, v45, v29
	v_fmac_f32_e32 v66, v46, v30
	v_fmac_f32_e32 v66, v47, v31
	ds_read_b128 v[32:35], v74 offset:4096
	ds_read_b128 v[36:39], v74 offset:4112
	ds_read_b128 v[40:43], v74 offset:4128
	ds_read_b128 v[44:47], v74 offset:4144
	s_waitcnt lgkmcnt(4)
	v_mul_f32_e32 v67, v48, v16
	v_fmac_f32_e32 v67, v49, v17
	v_fmac_f32_e32 v67, v50, v18
	v_fmac_f32_e32 v67, v51, v19
	v_fmac_f32_e32 v67, v52, v20
	v_fmac_f32_e32 v67, v53, v21
	v_fmac_f32_e32 v67, v54, v22
	v_fmac_f32_e32 v67, v55, v23
	v_fmac_f32_e32 v67, v56, v24
	v_fmac_f32_e32 v67, v57, v25
	v_fmac_f32_e32 v67, v58, v26
	v_fmac_f32_e32 v67, v59, v27
	v_fmac_f32_e32 v67, v60, v28
	v_fmac_f32_e32 v67, v61, v29
	v_fmac_f32_e32 v67, v62, v30
	v_fmac_f32_e32 v67, v63, v31
	ds_read_b128 v[48:51], v74 offset:5120
	ds_read_b128 v[52:55], v74 offset:5136
	ds_read_b128 v[56:59], v74 offset:5152
	ds_read_b128 v[60:63], v74 offset:5168
	s_waitcnt lgkmcnt(4)
	v_mul_f32_e32 v68, v32, v16
	v_fmac_f32_e32 v68, v33, v17
	v_fmac_f32_e32 v68, v34, v18
	v_fmac_f32_e32 v68, v35, v19
	v_fmac_f32_e32 v68, v36, v20
	v_fmac_f32_e32 v68, v37, v21
	v_fmac_f32_e32 v68, v38, v22
	v_fmac_f32_e32 v68, v39, v23
	v_fmac_f32_e32 v68, v40, v24
	v_fmac_f32_e32 v68, v41, v25
	v_fmac_f32_e32 v68, v42, v26
	v_fmac_f32_e32 v68, v43, v27
	v_fmac_f32_e32 v68, v44, v28
	v_fmac_f32_e32 v68, v45, v29
	v_fmac_f32_e32 v68, v46, v30
	v_fmac_f32_e32 v68, v47, v31
	ds_read_b128 v[32:35], v74 offset:6144
	ds_read_b128 v[36:39], v74 offset:6160
	ds_read_b128 v[40:43], v74 offset:6176
	ds_read_b128 v[44:47], v74 offset:6192
	s_waitcnt lgkmcnt(4)
	v_mul_f32_e32 v69, v48, v16
	v_fmac_f32_e32 v69, v49, v17
	v_fmac_f32_e32 v69, v50, v18
	v_fmac_f32_e32 v69, v51, v19
	v_fmac_f32_e32 v69, v52, v20
	v_fmac_f32_e32 v69, v53, v21
	v_fmac_f32_e32 v69, v54, v22
	v_fmac_f32_e32 v69, v55, v23
	v_fmac_f32_e32 v69, v56, v24
	v_fmac_f32_e32 v69, v57, v25
	v_fmac_f32_e32 v69, v58, v26
	v_fmac_f32_e32 v69, v59, v27
	v_fmac_f32_e32 v69, v60, v28
	v_fmac_f32_e32 v69, v61, v29
	v_fmac_f32_e32 v69, v62, v30
	v_fmac_f32_e32 v69, v63, v31
	ds_read_b128 v[48:51], v74 offset:7168
	ds_read_b128 v[52:55], v74 offset:7184
	ds_read_b128 v[56:59], v74 offset:7200
	ds_read_b128 v[60:63], v74 offset:7216
	s_waitcnt lgkmcnt(4)
	v_mul_f32_e32 v70, v32, v16
	v_fmac_f32_e32 v70, v33, v17
	v_fmac_f32_e32 v70, v34, v18
	v_fmac_f32_e32 v70, v35, v19
	v_fmac_f32_e32 v70, v36, v20
	v_fmac_f32_e32 v70, v37, v21
	v_fmac_f32_e32 v70, v38, v22
	v_fmac_f32_e32 v70, v39, v23
	v_fmac_f32_e32 v70, v40, v24
	v_fmac_f32_e32 v70, v41, v25
	v_fmac_f32_e32 v70, v42, v26
	v_fmac_f32_e32 v70, v43, v27
	v_fmac_f32_e32 v70, v44, v28
	v_fmac_f32_e32 v70, v45, v29
	v_fmac_f32_e32 v70, v46, v30
	v_fmac_f32_e32 v70, v47, v31
	s_waitcnt lgkmcnt(0)
	v_mul_f32_e32 v71, v48, v16
	v_fmac_f32_e32 v71, v49, v17
	v_fmac_f32_e32 v71, v50, v18
	v_fmac_f32_e32 v71, v51, v19
	v_fmac_f32_e32 v71, v52, v20
	v_fmac_f32_e32 v71, v53, v21
	v_fmac_f32_e32 v71, v54, v22
	v_fmac_f32_e32 v71, v55, v23
	v_fmac_f32_e32 v71, v56, v24
	v_fmac_f32_e32 v71, v57, v25
	v_fmac_f32_e32 v71, v58, v26
	v_fmac_f32_e32 v71, v59, v27
	v_fmac_f32_e32 v71, v60, v28
	v_fmac_f32_e32 v71, v61, v29
	v_fmac_f32_e32 v71, v62, v30
	v_fmac_f32_e32 v71, v63, v31
	ds_write_b32 v75, v64 offset:8192
	ds_write_b32 v75, v65 offset:8256
	ds_write_b32 v75, v66 offset:8320
	ds_write_b32 v75, v67 offset:8384
	ds_write_b32 v75, v68 offset:8448
	ds_write_b32 v75, v69 offset:8512
	ds_write_b32 v75, v70 offset:8576
	ds_write_b32 v75, v71 offset:8640
	s_lshr_b32 s22, s3, 1
	s_lshr_b32 s23, s22, 2
	s_mul_i32 s23, s23, 20
	s_and_b32 s24, s22, 3
	s_mul_i32 s24, s24, 5
	s_add_u32 s23, s23, s24
	s_and_b32 s25, s3, 1
	s_lshl_b32 s25, s25, 9
	s_lshr_b32 s26, s12, 1
	s_add_u32 s26, s26, s23
	s_lshl_b32 s26, s26, 10
	s_and_b32 s27, s12, 1
	s_lshl_b32 s27, s27, 8
	s_add_u32 s26, s26, s25
	s_add_u32 s26, s26, s27
	s_add_u32 s28, s10, s26
	s_addc_u32 s29, s11, 0
	s_add_u32 s30, s23, 4
	s_lshl_b32 s30, s30, 10
	s_add_u32 s30, s30, s25
	s_add_u32 s30, s10, s30
	s_addc_u32 s31, s11, 0
	s_waitcnt lgkmcnt(0)
	s_barrier
	v_cmp_gt_u32_e32 vcc, 0x80, v0
	s_and_saveexec_b64 s[32:33], vcc
	s_cbranch_execz .Lpre_A_main_done
	v_lshlrev_b32_e32 v76, 2, v0
	ds_read_b32 v32, v76 offset:8192
	ds_read_b32 v33, v76 offset:8704
	ds_read_b32 v34, v76 offset:9216
	ds_read_b32 v35, v76 offset:9728
	ds_read_b32 v36, v76 offset:10240
	ds_read_b32 v37, v76 offset:10752
	ds_read_b32 v38, v76 offset:11264
	ds_read_b32 v39, v76 offset:11776
	s_waitcnt lgkmcnt(0)
	ds_read_b32 v40, v76 offset:12288
	ds_read_b32 v41, v76 offset:12800
	ds_read_b32 v42, v76 offset:13312
	ds_read_b32 v43, v76 offset:13824
	ds_read_b32 v44, v76 offset:14336
	ds_read_b32 v45, v76 offset:14848
	ds_read_b32 v46, v76 offset:15360
	ds_read_b32 v47, v76 offset:15872
	s_waitcnt lgkmcnt(0)
	v_add_f32_e32 v32, v32, v33
	v_add_f32_e32 v32, v32, v34
	v_add_f32_e32 v32, v32, v35
	v_add_f32_e32 v32, v32, v36
	v_add_f32_e32 v32, v32, v37
	v_add_f32_e32 v32, v32, v38
	v_add_f32_e32 v32, v32, v39
	v_add_f32_e32 v32, v32, v40
	v_add_f32_e32 v32, v32, v41
	v_add_f32_e32 v32, v32, v42
	v_add_f32_e32 v32, v32, v43
	v_add_f32_e32 v32, v32, v44
	v_add_f32_e32 v32, v32, v45
	v_add_f32_e32 v32, v32, v46
	v_add_f32_e32 v32, v32, v47
	s_waitcnt vmcnt(0)
	v_mul_f32_e32 v32, v72, v32
	v_cvt_pk_bf16_f32 v32, v32, v32
	v_lshlrev_b32_e32 v77, 4, v1
	v_lshl_or_b32 v77, v2, 1, v77
	global_store_short v77, v32, s[28:29]
.Lpre_A_main_done:
	s_or_b64 exec, exec, s[32:33]
	s_cmp_lg_u32 s12, 0
	s_cbranch_scc1 .Lpre_A_done
	v_mov_b32_e32 v78, 0
	v_cmp_gt_u32_e32 vcc, 64, v0
	s_and_saveexec_b64 s[32:33], vcc
	s_cbranch_execz .Lpre_A_sum_done
	v_and_b32_e32 v79, 7, v0
	v_lshlrev_b32_e32 v79, 10, v79
	v_lshrrev_b32_e32 v80, 3, v0
	v_lshl_or_b32 v79, v80, 7, v79
	ds_read_b128 v[32:35], v79 offset:0
	ds_read_b128 v[36:39], v79 offset:16
	ds_read_b128 v[40:43], v79 offset:32
	ds_read_b128 v[44:47], v79 offset:48
	ds_read_b128 v[48:51], v79 offset:64
	ds_read_b128 v[52:55], v79 offset:80
	ds_read_b128 v[56:59], v79 offset:96
	ds_read_b128 v[60:63], v79 offset:112
	s_waitcnt lgkmcnt(0)
	v_add_f32_e32 v78, 0, v32
	v_add_f32_e32 v78, v78, v33
	v_add_f32_e32 v78, v78, v34
	v_add_f32_e32 v78, v78, v35
	v_add_f32_e32 v78, v78, v36
	v_add_f32_e32 v78, v78, v37
	v_add_f32_e32 v78, v78, v38
	v_add_f32_e32 v78, v78, v39
	v_add_f32_e32 v78, v78, v40
	v_add_f32_e32 v78, v78, v41
	v_add_f32_e32 v78, v78, v42
	v_add_f32_e32 v78, v78, v43
	v_add_f32_e32 v78, v78, v44
	v_add_f32_e32 v78, v78, v45
	v_add_f32_e32 v78, v78, v46
	v_add_f32_e32 v78, v78, v47
	v_add_f32_e32 v78, v78, v48
	v_add_f32_e32 v78, v78, v49
	v_add_f32_e32 v78, v78, v50
	v_add_f32_e32 v78, v78, v51
	v_add_f32_e32 v78, v78, v52
	v_add_f32_e32 v78, v78, v53
	v_add_f32_e32 v78, v78, v54
	v_add_f32_e32 v78, v78, v55
	v_add_f32_e32 v78, v78, v56
	v_add_f32_e32 v78, v78, v57
	v_add_f32_e32 v78, v78, v58
	v_add_f32_e32 v78, v78, v59
	v_add_f32_e32 v78, v78, v60
	v_add_f32_e32 v78, v78, v61
	v_add_f32_e32 v78, v78, v62
	v_add_f32_e32 v78, v78, v63
	s_waitcnt vmcnt(0)
	v_mul_f32_e32 v78, v73, v78
.Lpre_A_sum_done:
	s_or_b64 exec, exec, s[32:33]
	v_cvt_pk_bf16_f32 v78, v78, v78
	v_lshlrev_b32_e32 v81, 1, v0
	global_store_short v81, v78, s[30:31]

.Lpre_roleE:
	s_sub_u32 s3, s2, 0xad
	s_cmp_gt_u32 s3, 191
	s_cbranch_scc1 .Lpre_E_exit
	s_load_dwordx16 s[4:19], s[0:1], 0x68
	s_load_dwordx2 s[20:21], s[0:1], 0xa8
	s_mul_hi_u32 s22, s3, 0xaaaaaaab
	s_lshr_b32 s22, s22, 3
	s_mul_i32 s23, s22, 12
	s_sub_u32 s23, s3, s23
	s_lshr_b32 s24, s23, 2
	s_and_b32 s25, s23, 3
	s_lshl_b32 s25, s25, 6
	v_and_b32_e32 v1, 63, v0
	v_lshrrev_b32_e32 v62, 6, v0
	v_and_b32_e32 v2, 15, v0
	v_bfe_u32 v3, v0, 4, 2
	v_readfirstlane_b32 s26, v62
	s_cmp_lt_u32 s24, 2
	s_cselect_b32 s28, 14, 13
	s_lshl_b32 s27, 1, s28
	s_lshr_b32 s27, s27, 3
	v_lshlrev_b32_e32 v4, s28, v3
	v_lshl_or_b32 v4, v62, 6, v4
	v_lshl_or_b32 v4, v2, 2, v4
	v_add_u32_e32 v5, s27, v4
	v_add_u32_e32 v6, s27, v5
	v_add_u32_e32 v7, s27, v6
	v_add_u32_e32 v8, s27, v7
	v_add_u32_e32 v9, s27, v8
	v_add_u32_e32 v10, s27, v9
	v_add_u32_e32 v11, s27, v10
	v_lshlrev_b32_e32 v12, 4, v1
	v_add_u32_e32 v13, 0x1000, v12
	s_lshl_b32 s29, s22, 15
	s_lshl_b32 s30, s26, 13
	s_add_u32 s29, s29, s30
	s_waitcnt lgkmcnt(0)
	s_add_u32 s32, s4, s29
	s_addc_u32 s33, s5, 0
	global_load_dwordx4 v[16:19], v12, s[32:33]
	global_load_dwordx4 v[20:23], v12, s[32:33] offset:1024
	global_load_dwordx4 v[24:27], v12, s[32:33] offset:2048
	global_load_dwordx4 v[28:31], v12, s[32:33] offset:3072
	global_load_dwordx4 v[32:35], v13, s[32:33]
	global_load_dwordx4 v[36:39], v13, s[32:33] offset:1024
	global_load_dwordx4 v[40:43], v13, s[32:33] offset:2048
	global_load_dwordx4 v[44:47], v13, s[32:33] offset:3072
	global_load_dwordx4 v[48:51], v12, s[6:7]
	global_load_dwordx4 v[52:55], v12, s[8:9]
	s_cmp_lt_u32 s24, 2
	s_cselect_b32 s34, s10, s12
	s_cselect_b32 s35, s11, s13
	s_and_b32 s36, s24, 1
	s_lshl_b32 s36, s36, 10
	s_lshl_b32 s37, s25, 2
	s_add_u32 s36, s36, s37
	s_add_u32 s34, s34, s36
	s_addc_u32 s35, s35, 0
	s_lshl_b32 s38, s27, 5
	s_mov_b64 s[40:41], s[34:35]
	s_add_u32 s42, s40, s38
	s_addc_u32 s43, s41, 0
	s_add_u32 s44, s42, s38
	s_addc_u32 s45, s43, 0
	s_add_u32 s46, s44, s38
	s_addc_u32 s47, s45, 0
	s_add_u32 s48, s46, s38
	s_addc_u32 s49, s47, 0
	s_add_u32 s50, s48, s38
	s_addc_u32 s51, s49, 0
	s_add_u32 s52, s50, s38
	s_addc_u32 s53, s51, 0
	s_add_u32 s54, s52, s38
	s_addc_u32 s55, s53, 0
	global_load_dword v64, v4, s[40:41]
	global_load_dword v65, v5, s[40:41]
	global_load_dword v66, v6, s[40:41]
	global_load_dword v67, v7, s[40:41]
	global_load_dword v68, v8, s[40:41]
	global_load_dword v69, v9, s[40:41]
	global_load_dword v70, v10, s[40:41]
	global_load_dword v71, v11, s[40:41]
	global_load_dword v72, v4, s[42:43]
	global_load_dword v73, v5, s[42:43]
	global_load_dword v74, v6, s[42:43]
	global_load_dword v75, v7, s[42:43]
	global_load_dword v76, v8, s[42:43]
	global_load_dword v77, v9, s[42:43]
	global_load_dword v78, v10, s[42:43]
	global_load_dword v79, v11, s[42:43]
	global_load_dword v80, v4, s[44:45]
	global_load_dword v81, v5, s[44:45]
	global_load_dword v82, v6, s[44:45]
	global_load_dword v83, v7, s[44:45]
	global_load_dword v84, v8, s[44:45]
	global_load_dword v85, v9, s[44:45]
	global_load_dword v86, v10, s[44:45]
	global_load_dword v87, v11, s[44:45]
	global_load_dword v88, v4, s[46:47]
	global_load_dword v89, v5, s[46:47]
	global_load_dword v90, v6, s[46:47]
	global_load_dword v91, v7, s[46:47]
	global_load_dword v92, v8, s[46:47]
	global_load_dword v93, v9, s[46:47]
	global_load_dword v94, v10, s[46:47]
	global_load_dword v95, v11, s[46:47]
	global_load_dword v96, v4, s[48:49]
	global_load_dword v97, v5, s[48:49]
	global_load_dword v98, v6, s[48:49]
	global_load_dword v99, v7, s[48:49]
	global_load_dword v100, v8, s[48:49]
	global_load_dword v101, v9, s[48:49]
	global_load_dword v102, v10, s[48:49]
	global_load_dword v103, v11, s[48:49]
	global_load_dword v104, v4, s[50:51]
	global_load_dword v105, v5, s[50:51]
	global_load_dword v106, v6, s[50:51]
	global_load_dword v107, v7, s[50:51]
	global_load_dword v108, v8, s[50:51]
	global_load_dword v109, v9, s[50:51]
	global_load_dword v110, v10, s[50:51]
	global_load_dword v111, v11, s[50:51]
	global_load_dword v112, v4, s[52:53]
	global_load_dword v113, v5, s[52:53]
	global_load_dword v114, v6, s[52:53]
	global_load_dword v115, v7, s[52:53]
	global_load_dword v116, v8, s[52:53]
	global_load_dword v117, v9, s[52:53]
	global_load_dword v118, v10, s[52:53]
	global_load_dword v119, v11, s[52:53]
	global_load_dword v120, v4, s[54:55]
	global_load_dword v121, v5, s[54:55]
	global_load_dword v122, v6, s[54:55]
	global_load_dword v123, v7, s[54:55]
	global_load_dword v124, v8, s[54:55]
	global_load_dword v125, v9, s[54:55]
	global_load_dword v126, v10, s[54:55]
	global_load_dword v127, v11, s[54:55]
	v_lshlrev_b32_e32 v14, 6, v62
	v_lshl_or_b32 v14, v3, 4, v14
	s_lshl_b32 s37, s25, 2
	s_add_u32 s56, s14, s37
	s_addc_u32 s57, s15, 0
	global_load_dwordx4 v[56:59], v14, s[56:57]
	s_waitcnt vmcnt(63)
	v_add_f32_e32 v4, v16, v17
	v_add_f32_e32 v5, v20, v21
	v_add_f32_e32 v6, v24, v25
	v_add_f32_e32 v7, v28, v29
	v_add_f32_e32 v8, v32, v33
	v_add_f32_e32 v9, v36, v37
	v_add_f32_e32 v10, v40, v41
	v_add_f32_e32 v11, v44, v45
	v_add_f32_e32 v4, v4, v18
	v_add_f32_e32 v5, v5, v22
	v_add_f32_e32 v6, v6, v26
	v_add_f32_e32 v7, v7, v30
	v_add_f32_e32 v8, v8, v34
	v_add_f32_e32 v9, v9, v38
	v_add_f32_e32 v10, v10, v42
	v_add_f32_e32 v11, v11, v46
	v_add_f32_e32 v4, v4, v19
	v_add_f32_e32 v5, v5, v23
	v_add_f32_e32 v6, v6, v27
	v_add_f32_e32 v7, v7, v31
	v_add_f32_e32 v8, v8, v35
	v_add_f32_e32 v9, v9, v39
	v_add_f32_e32 v10, v10, v43
	v_add_f32_e32 v11, v11, v47
	s_nop 1
	v_add_f32_dpp v4, v4, v4 quad_perm:[1,0,3,2] row_mask:0xf bank_mask:0xf
	v_add_f32_dpp v5, v5, v5 quad_perm:[1,0,3,2] row_mask:0xf bank_mask:0xf
	v_add_f32_dpp v6, v6, v6 quad_perm:[1,0,3,2] row_mask:0xf bank_mask:0xf
	v_add_f32_dpp v7, v7, v7 quad_perm:[1,0,3,2] row_mask:0xf bank_mask:0xf
	s_nop 1
	v_add_f32_dpp v4, v4, v4 quad_perm:[2,3,0,1] row_mask:0xf bank_mask:0xf
	v_add_f32_dpp v5, v5, v5 quad_perm:[2,3,0,1] row_mask:0xf bank_mask:0xf
	v_add_f32_dpp v6, v6, v6 quad_perm:[2,3,0,1] row_mask:0xf bank_mask:0xf
	v_add_f32_dpp v7, v7, v7 quad_perm:[2,3,0,1] row_mask:0xf bank_mask:0xf
	s_nop 1
	v_add_f32_dpp v4, v4, v4 row_half_mirror row_mask:0xf bank_mask:0xf
	v_add_f32_dpp v5, v5, v5 row_half_mirror row_mask:0xf bank_mask:0xf
	v_add_f32_dpp v6, v6, v6 row_half_mirror row_mask:0xf bank_mask:0xf
	v_add_f32_dpp v7, v7, v7 row_half_mirror row_mask:0xf bank_mask:0xf
	s_nop 1
	v_add_f32_dpp v4, v4, v4 row_mirror row_mask:0xf bank_mask:0xf
	v_add_f32_dpp v5, v5, v5 row_mirror row_mask:0xf bank_mask:0xf
	v_add_f32_dpp v6, v6, v6 row_mirror row_mask:0xf bank_mask:0xf
	v_add_f32_dpp v7, v7, v7 row_mirror row_mask:0xf bank_mask:0xf
	s_nop 1
	v_mov_b32_e32 v60, v4
	v_mov_b32_e32 v61, v5
	v_mov_b32_e32 v63, v6
	v_mov_b32_e32 v15, v7
	s_nop 1
	v_permlane16_swap_b32_e32 v4, v60
	v_permlane16_swap_b32_e32 v5, v61
	v_permlane16_swap_b32_e32 v6, v63
	v_permlane16_swap_b32_e32 v7, v15
	v_add_f32_e32 v4, v4, v60
	v_add_f32_e32 v5, v5, v61
	v_add_f32_e32 v6, v6, v63
	v_add_f32_e32 v7, v7, v15
	v_mov_b32_e32 v60, v4
	v_mov_b32_e32 v61, v5
	v_mov_b32_e32 v63, v6
	v_mov_b32_e32 v15, v7
	s_nop 1
	v_permlane32_swap_b32_e32 v4, v60
	v_permlane32_swap_b32_e32 v5, v61
	v_permlane32_swap_b32_e32 v6, v63
	v_permlane32_swap_b32_e32 v7, v15
	v_add_f32_e32 v4, v4, v60
	v_add_f32_e32 v5, v5, v61
	v_add_f32_e32 v6, v6, v63
	v_add_f32_e32 v7, v7, v15
	v_add_f32_dpp v8, v8, v8 quad_perm:[1,0,3,2] row_mask:0xf bank_mask:0xf
	v_add_f32_dpp v9, v9, v9 quad_perm:[1,0,3,2] row_mask:0xf bank_mask:0xf
	v_add_f32_dpp v10, v10, v10 quad_perm:[1,0,3,2] row_mask:0xf bank_mask:0xf
	v_add_f32_dpp v11, v11, v11 quad_perm:[1,0,3,2] row_mask:0xf bank_mask:0xf
	s_nop 1
	v_add_f32_dpp v8, v8, v8 quad_perm:[2,3,0,1] row_mask:0xf bank_mask:0xf
	v_add_f32_dpp v9, v9, v9 quad_perm:[2,3,0,1] row_mask:0xf bank_mask:0xf
	v_add_f32_dpp v10, v10, v10 quad_perm:[2,3,0,1] row_mask:0xf bank_mask:0xf
	v_add_f32_dpp v11, v11, v11 quad_perm:[2,3,0,1] row_mask:0xf bank_mask:0xf
	s_nop 1
	v_add_f32_dpp v8, v8, v8 row_half_mirror row_mask:0xf bank_mask:0xf
	v_add_f32_dpp v9, v9, v9 row_half_mirror row_mask:0xf bank_mask:0xf
	v_add_f32_dpp v10, v10, v10 row_half_mirror row_mask:0xf bank_mask:0xf
	v_add_f32_dpp v11, v11, v11 row_half_mirror row_mask:0xf bank_mask:0xf
	s_nop 1
	v_add_f32_dpp v8, v8, v8 row_mirror row_mask:0xf bank_mask:0xf
	v_add_f32_dpp v9, v9, v9 row_mirror row_mask:0xf bank_mask:0xf
	v_add_f32_dpp v10, v10, v10 row_mirror row_mask:0xf bank_mask:0xf
	v_add_f32_dpp v11, v11, v11 row_mirror row_mask:0xf bank_mask:0xf
	s_nop 1
	v_mov_b32_e32 v60, v8
	v_mov_b32_e32 v61, v9
	v_mov_b32_e32 v63, v10
	v_mov_b32_e32 v15, v11
	s_nop 1
	v_permlane16_swap_b32_e32 v8, v60
	v_permlane16_swap_b32_e32 v9, v61
	v_permlane16_swap_b32_e32 v10, v63
	v_permlane16_swap_b32_e32 v11, v15
	v_add_f32_e32 v8, v8, v60
	v_add_f32_e32 v9, v9, v61
	v_add_f32_e32 v10, v10, v63
	v_add_f32_e32 v11, v11, v15
	v_mov_b32_e32 v60, v8
	v_mov_b32_e32 v61, v9
	v_mov_b32_e32 v63, v10
	v_mov_b32_e32 v15, v11
	s_nop 1
	v_permlane32_swap_b32_e32 v8, v60
	v_permlane32_swap_b32_e32 v9, v61
	v_permlane32_swap_b32_e32 v10, v63
	v_permlane32_swap_b32_e32 v11, v15
	v_add_f32_e32 v8, v8, v60
	v_add_f32_e32 v9, v9, v61
	v_add_f32_e32 v10, v10, v63
	v_add_f32_e32 v11, v11, v15
	v_mul_f32_e32 v4, 0x3b800000, v4
	v_mul_f32_e32 v5, 0x3b800000, v5
	v_mul_f32_e32 v6, 0x3b800000, v6
	v_mul_f32_e32 v7, 0x3b800000, v7
	v_mul_f32_e32 v8, 0x3b800000, v8
	v_mul_f32_e32 v9, 0x3b800000, v9
	v_mul_f32_e32 v10, 0x3b800000, v10
	v_mul_f32_e32 v11, 0x3b800000, v11
	v_sub_f32_e32 v16, v16, v4
	v_sub_f32_e32 v17, v17, v4
	v_sub_f32_e32 v18, v18, v4
	v_sub_f32_e32 v19, v19, v4
	v_sub_f32_e32 v20, v20, v5
	v_sub_f32_e32 v21, v21, v5
	v_sub_f32_e32 v22, v22, v5
	v_sub_f32_e32 v23, v23, v5
	v_sub_f32_e32 v24, v24, v6
	v_sub_f32_e32 v25, v25, v6
	v_sub_f32_e32 v26, v26, v6
	v_sub_f32_e32 v27, v27, v6
	v_sub_f32_e32 v28, v28, v7
	v_sub_f32_e32 v29, v29, v7
	v_sub_f32_e32 v30, v30, v7
	v_sub_f32_e32 v31, v31, v7
	v_sub_f32_e32 v32, v32, v8
	v_sub_f32_e32 v33, v33, v8
	v_sub_f32_e32 v34, v34, v8
	v_sub_f32_e32 v35, v35, v8
	v_sub_f32_e32 v36, v36, v9
	v_sub_f32_e32 v37, v37, v9
	v_sub_f32_e32 v38, v38, v9
	v_sub_f32_e32 v39, v39, v9
	v_sub_f32_e32 v40, v40, v10
	v_sub_f32_e32 v41, v41, v10
	v_sub_f32_e32 v42, v42, v10
	v_sub_f32_e32 v43, v43, v10
	v_sub_f32_e32 v44, v44, v11
	v_sub_f32_e32 v45, v45, v11
	v_sub_f32_e32 v46, v46, v11
	v_sub_f32_e32 v47, v47, v11
	v_mul_f32_e32 v4, v16, v16
	v_mul_f32_e32 v5, v20, v20
	v_mul_f32_e32 v6, v24, v24
	v_mul_f32_e32 v7, v28, v28
	v_mul_f32_e32 v8, v32, v32
	v_mul_f32_e32 v9, v36, v36
	v_mul_f32_e32 v10, v40, v40
	v_mul_f32_e32 v11, v44, v44
	v_fmac_f32_e32 v4, v17, v17
	v_fmac_f32_e32 v5, v21, v21
	v_fmac_f32_e32 v6, v25, v25
	v_fmac_f32_e32 v7, v29, v29
	v_fmac_f32_e32 v8, v33, v33
	v_fmac_f32_e32 v9, v37, v37
	v_fmac_f32_e32 v10, v41, v41
	v_fmac_f32_e32 v11, v45, v45
	v_fmac_f32_e32 v4, v18, v18
	v_fmac_f32_e32 v5, v22, v22
	v_fmac_f32_e32 v6, v26, v26
	v_fmac_f32_e32 v7, v30, v30
	v_fmac_f32_e32 v8, v34, v34
	v_fmac_f32_e32 v9, v38, v38
	v_fmac_f32_e32 v10, v42, v42
	v_fmac_f32_e32 v11, v46, v46
	v_fmac_f32_e32 v4, v19, v19
	v_fmac_f32_e32 v5, v23, v23
	v_fmac_f32_e32 v6, v27, v27
	v_fmac_f32_e32 v7, v31, v31
	v_fmac_f32_e32 v8, v35, v35
	v_fmac_f32_e32 v9, v39, v39
	v_fmac_f32_e32 v10, v43, v43
	v_fmac_f32_e32 v11, v47, v47
	s_nop 1
	v_add_f32_dpp v4, v4, v4 quad_perm:[1,0,3,2] row_mask:0xf bank_mask:0xf
	v_add_f32_dpp v5, v5, v5 quad_perm:[1,0,3,2] row_mask:0xf bank_mask:0xf
	v_add_f32_dpp v6, v6, v6 quad_perm:[1,0,3,2] row_mask:0xf bank_mask:0xf
	v_add_f32_dpp v7, v7, v7 quad_perm:[1,0,3,2] row_mask:0xf bank_mask:0xf
	s_nop 1
	v_add_f32_dpp v4, v4, v4 quad_perm:[2,3,0,1] row_mask:0xf bank_mask:0xf
	v_add_f32_dpp v5, v5, v5 quad_perm:[2,3,0,1] row_mask:0xf bank_mask:0xf
	v_add_f32_dpp v6, v6, v6 quad_perm:[2,3,0,1] row_mask:0xf bank_mask:0xf
	v_add_f32_dpp v7, v7, v7 quad_perm:[2,3,0,1] row_mask:0xf bank_mask:0xf
	s_nop 1
	v_add_f32_dpp v4, v4, v4 row_half_mirror row_mask:0xf bank_mask:0xf
	v_add_f32_dpp v5, v5, v5 row_half_mirror row_mask:0xf bank_mask:0xf
	v_add_f32_dpp v6, v6, v6 row_half_mirror row_mask:0xf bank_mask:0xf
	v_add_f32_dpp v7, v7, v7 row_half_mirror row_mask:0xf bank_mask:0xf
	s_nop 1
	v_add_f32_dpp v4, v4, v4 row_mirror row_mask:0xf bank_mask:0xf
	v_add_f32_dpp v5, v5, v5 row_mirror row_mask:0xf bank_mask:0xf
	v_add_f32_dpp v6, v6, v6 row_mirror row_mask:0xf bank_mask:0xf
	v_add_f32_dpp v7, v7, v7 row_mirror row_mask:0xf bank_mask:0xf
	s_nop 1
	v_mov_b32_e32 v60, v4
	v_mov_b32_e32 v61, v5
	v_mov_b32_e32 v63, v6
	v_mov_b32_e32 v15, v7
	s_nop 1
	v_permlane16_swap_b32_e32 v4, v60
	v_permlane16_swap_b32_e32 v5, v61
	v_permlane16_swap_b32_e32 v6, v63
	v_permlane16_swap_b32_e32 v7, v15
	v_add_f32_e32 v4, v4, v60
	v_add_f32_e32 v5, v5, v61
	v_add_f32_e32 v6, v6, v63
	v_add_f32_e32 v7, v7, v15
	v_mov_b32_e32 v60, v4
	v_mov_b32_e32 v61, v5
	v_mov_b32_e32 v63, v6
	v_mov_b32_e32 v15, v7
	s_nop 1
	v_permlane32_swap_b32_e32 v4, v60
	v_permlane32_swap_b32_e32 v5, v61
	v_permlane32_swap_b32_e32 v6, v63
	v_permlane32_swap_b32_e32 v7, v15
	v_add_f32_e32 v4, v4, v60
	v_add_f32_e32 v5, v5, v61
	v_add_f32_e32 v6, v6, v63
	v_add_f32_e32 v7, v7, v15
	v_add_f32_dpp v8, v8, v8 quad_perm:[1,0,3,2] row_mask:0xf bank_mask:0xf
	v_add_f32_dpp v9, v9, v9 quad_perm:[1,0,3,2] row_mask:0xf bank_mask:0xf
	v_add_f32_dpp v10, v10, v10 quad_perm:[1,0,3,2] row_mask:0xf bank_mask:0xf
	v_add_f32_dpp v11, v11, v11 quad_perm:[1,0,3,2] row_mask:0xf bank_mask:0xf
	s_nop 1
	v_add_f32_dpp v8, v8, v8 quad_perm:[2,3,0,1] row_mask:0xf bank_mask:0xf
	v_add_f32_dpp v9, v9, v9 quad_perm:[2,3,0,1] row_mask:0xf bank_mask:0xf
	v_add_f32_dpp v10, v10, v10 quad_perm:[2,3,0,1] row_mask:0xf bank_mask:0xf
	v_add_f32_dpp v11, v11, v11 quad_perm:[2,3,0,1] row_mask:0xf bank_mask:0xf
	s_nop 1
	v_add_f32_dpp v8, v8, v8 row_half_mirror row_mask:0xf bank_mask:0xf
	v_add_f32_dpp v9, v9, v9 row_half_mirror row_mask:0xf bank_mask:0xf
	v_add_f32_dpp v10, v10, v10 row_half_mirror row_mask:0xf bank_mask:0xf
	v_add_f32_dpp v11, v11, v11 row_half_mirror row_mask:0xf bank_mask:0xf
	s_nop 1
	v_add_f32_dpp v8, v8, v8 row_mirror row_mask:0xf bank_mask:0xf
	v_add_f32_dpp v9, v9, v9 row_mirror row_mask:0xf bank_mask:0xf
	v_add_f32_dpp v10, v10, v10 row_mirror row_mask:0xf bank_mask:0xf
	v_add_f32_dpp v11, v11, v11 row_mirror row_mask:0xf bank_mask:0xf
	s_nop 1
	v_mov_b32_e32 v60, v8
	v_mov_b32_e32 v61, v9
	v_mov_b32_e32 v63, v10
	v_mov_b32_e32 v15, v11
	s_nop 1
	v_permlane16_swap_b32_e32 v8, v60
	v_permlane16_swap_b32_e32 v9, v61
	v_permlane16_swap_b32_e32 v10, v63
	v_permlane16_swap_b32_e32 v11, v15
	v_add_f32_e32 v8, v8, v60
	v_add_f32_e32 v9, v9, v61
	v_add_f32_e32 v10, v10, v63
	v_add_f32_e32 v11, v11, v15
	v_mov_b32_e32 v60, v8
	v_mov_b32_e32 v61, v9
	v_mov_b32_e32 v63, v10
	v_mov_b32_e32 v15, v11
	s_nop 1
	v_permlane32_swap_b32_e32 v8, v60
	v_permlane32_swap_b32_e32 v9, v61
	v_permlane32_swap_b32_e32 v10, v63
	v_permlane32_swap_b32_e32 v11, v15
	v_add_f32_e32 v8, v8, v60
	v_add_f32_e32 v9, v9, v61
	v_add_f32_e32 v10, v10, v63
	v_add_f32_e32 v11, v11, v15
	v_mov_b32_e32 v60, 0x3727c5ac
	v_mul_f32_e32 v4, 0x3b800000, v4
	v_mul_f32_e32 v5, 0x3b800000, v5
	v_mul_f32_e32 v6, 0x3b800000, v6
	v_mul_f32_e32 v7, 0x3b800000, v7
	v_mul_f32_e32 v8, 0x3b800000, v8
	v_mul_f32_e32 v9, 0x3b800000, v9
	v_mul_f32_e32 v10, 0x3b800000, v10
	v_mul_f32_e32 v11, 0x3b800000, v11
	v_add_f32_e32 v4, v4, v60
	v_add_f32_e32 v5, v5, v60
	v_add_f32_e32 v6, v6, v60
	v_add_f32_e32 v7, v7, v60
	v_add_f32_e32 v8, v8, v60
	v_add_f32_e32 v9, v9, v60
	v_add_f32_e32 v10, v10, v60
	v_add_f32_e32 v11, v11, v60
	v_rsq_f32_e32 v4, v4
	v_rsq_f32_e32 v5, v5
	v_rsq_f32_e32 v6, v6
	v_rsq_f32_e32 v7, v7
	v_rsq_f32_e32 v8, v8
	v_rsq_f32_e32 v9, v9
	v_rsq_f32_e32 v10, v10
	v_rsq_f32_e32 v11, v11
	s_nop 0
	v_mul_f32_e32 v16, v16, v4
	v_mul_f32_e32 v17, v17, v4
	v_mul_f32_e32 v18, v18, v4
	v_mul_f32_e32 v19, v19, v4
	v_mul_f32_e32 v20, v20, v5
	v_mul_f32_e32 v21, v21, v5
	v_mul_f32_e32 v22, v22, v5
	v_mul_f32_e32 v23, v23, v5
	v_mul_f32_e32 v24, v24, v6
	v_mul_f32_e32 v25, v25, v6
	v_mul_f32_e32 v26, v26, v6
	v_mul_f32_e32 v27, v27, v6
	v_mul_f32_e32 v28, v28, v7
	v_mul_f32_e32 v29, v29, v7
	v_mul_f32_e32 v30, v30, v7
	v_mul_f32_e32 v31, v31, v7
	v_mul_f32_e32 v32, v32, v8
	v_mul_f32_e32 v33, v33, v8
	v_mul_f32_e32 v34, v34, v8
	v_mul_f32_e32 v35, v35, v8
	v_mul_f32_e32 v36, v36, v9
	v_mul_f32_e32 v37, v37, v9
	v_mul_f32_e32 v38, v38, v9
	v_mul_f32_e32 v39, v39, v9
	v_mul_f32_e32 v40, v40, v10
	v_mul_f32_e32 v41, v41, v10
	v_mul_f32_e32 v42, v42, v10
	v_mul_f32_e32 v43, v43, v10
	v_mul_f32_e32 v44, v44, v11
	v_mul_f32_e32 v45, v45, v11
	v_mul_f32_e32 v46, v46, v11
	v_mul_f32_e32 v47, v47, v11
	v_fma_f32 v16, v16, v48, v52
	v_fma_f32 v17, v17, v49, v53
	v_fma_f32 v18, v18, v50, v54
	v_fma_f32 v19, v19, v51, v55
	v_fma_f32 v20, v20, v48, v52
	v_fma_f32 v21, v21, v49, v53
	v_fma_f32 v22, v22, v50, v54
	v_fma_f32 v23, v23, v51, v55
	v_fma_f32 v24, v24, v48, v52
	v_fma_f32 v25, v25, v49, v53
	v_fma_f32 v26, v26, v50, v54
	v_fma_f32 v27, v27, v51, v55
	v_fma_f32 v28, v28, v48, v52
	v_fma_f32 v29, v29, v49, v53
	v_fma_f32 v30, v30, v50, v54
	v_fma_f32 v31, v31, v51, v55
	v_fma_f32 v32, v32, v48, v52
	v_fma_f32 v33, v33, v49, v53
	v_fma_f32 v34, v34, v50, v54
	v_fma_f32 v35, v35, v51, v55
	v_fma_f32 v36, v36, v48, v52
	v_fma_f32 v37, v37, v49, v53
	v_fma_f32 v38, v38, v50, v54
	v_fma_f32 v39, v39, v51, v55
	v_fma_f32 v40, v40, v48, v52
	v_fma_f32 v41, v41, v49, v53
	v_fma_f32 v42, v42, v50, v54
	v_fma_f32 v43, v43, v51, v55
	v_fma_f32 v44, v44, v48, v52
	v_fma_f32 v45, v45, v49, v53
	v_fma_f32 v46, v46, v50, v54
	v_fma_f32 v47, v47, v51, v55
	v_lshlrev_b32_e32 v61, 3, v1
	s_mul_i32 s31, s26, 4224
	v_add_u32_e32 v61, s31, v61
	v_cvt_pk_bf16_f32 v16, v16, v17
	v_cvt_pk_bf16_f32 v17, v18, v19
	ds_write_b64 v61, v[16:17]
	v_cvt_pk_bf16_f32 v20, v20, v21
	v_cvt_pk_bf16_f32 v21, v22, v23
	ds_write_b64 v61, v[20:21] offset:528
	v_cvt_pk_bf16_f32 v24, v24, v25
	v_cvt_pk_bf16_f32 v25, v26, v27
	ds_write_b64 v61, v[24:25] offset:1056
	v_cvt_pk_bf16_f32 v28, v28, v29
	v_cvt_pk_bf16_f32 v29, v30, v31
	ds_write_b64 v61, v[28:29] offset:1584
	v_cvt_pk_bf16_f32 v32, v32, v33
	v_cvt_pk_bf16_f32 v33, v34, v35
	ds_write_b64 v61, v[32:33] offset:2112
	v_cvt_pk_bf16_f32 v36, v36, v37
	v_cvt_pk_bf16_f32 v37, v38, v39
	ds_write_b64 v61, v[36:37] offset:2640
	v_cvt_pk_bf16_f32 v40, v40, v41
	v_cvt_pk_bf16_f32 v41, v42, v43
	ds_write_b64 v61, v[40:41] offset:3168
	v_cvt_pk_bf16_f32 v44, v44, v45
	v_cvt_pk_bf16_f32 v45, v46, v47
	ds_write_b64 v61, v[44:45] offset:3696
	v_mul_u32_u24_e32 v63, 528, v2
	v_lshlrev_b32_e32 v60, 4, v3
	v_add_u32_e32 v63, v63, v60
	s_waitcnt lgkmcnt(0)
	s_barrier
	s_waitcnt vmcnt(1)
	v_cvt_pk_bf16_f32 v64, v64, v65
	v_cvt_pk_bf16_f32 v65, v66, v67
	v_cvt_pk_bf16_f32 v66, v68, v69
	v_cvt_pk_bf16_f32 v67, v70, v71
	v_cvt_pk_bf16_f32 v72, v72, v73
	v_cvt_pk_bf16_f32 v73, v74, v75
	v_cvt_pk_bf16_f32 v74, v76, v77
	v_cvt_pk_bf16_f32 v75, v78, v79
	v_cvt_pk_bf16_f32 v80, v80, v81
	v_cvt_pk_bf16_f32 v81, v82, v83
	v_cvt_pk_bf16_f32 v82, v84, v85
	v_cvt_pk_bf16_f32 v83, v86, v87
	v_cvt_pk_bf16_f32 v88, v88, v89
	v_cvt_pk_bf16_f32 v89, v90, v91
	v_cvt_pk_bf16_f32 v90, v92, v93
	v_cvt_pk_bf16_f32 v91, v94, v95
	v_cvt_pk_bf16_f32 v96, v96, v97
	v_cvt_pk_bf16_f32 v97, v98, v99
	v_cvt_pk_bf16_f32 v98, v100, v101
	v_cvt_pk_bf16_f32 v99, v102, v103
	v_cvt_pk_bf16_f32 v104, v104, v105
	v_cvt_pk_bf16_f32 v105, v106, v107
	v_cvt_pk_bf16_f32 v106, v108, v109
	v_cvt_pk_bf16_f32 v107, v110, v111
	v_cvt_pk_bf16_f32 v112, v112, v113
	v_cvt_pk_bf16_f32 v113, v114, v115
	v_cvt_pk_bf16_f32 v114, v116, v117
	v_cvt_pk_bf16_f32 v115, v118, v119
	v_cvt_pk_bf16_f32 v120, v120, v121
	v_cvt_pk_bf16_f32 v121, v122, v123
	v_cvt_pk_bf16_f32 v122, v124, v125
	v_cvt_pk_bf16_f32 v123, v126, v127
	ds_read_b128 v[16:19], v63 offset:0
	ds_read_b128 v[20:23], v63 offset:8448
	ds_read_b128 v[24:27], v63 offset:64
	ds_read_b128 v[28:31], v63 offset:8512
	ds_read_b128 v[32:35], v63 offset:128
	ds_read_b128 v[36:39], v63 offset:8576
	ds_read_b128 v[40:43], v63 offset:192
	ds_read_b128 v[44:47], v63 offset:8640
	s_waitcnt lgkmcnt(0)
	v_mfma_f32_16x16x32_bf16 v[48:51], v[64:67], v[16:19], 0
	v_mfma_f32_16x16x32_bf16 v[52:55], v[64:67], v[20:23], 0
	v_mfma_f32_16x16x32_bf16 v[48:51], v[72:75], v[24:27], v[48:51]
	v_mfma_f32_16x16x32_bf16 v[52:55], v[72:75], v[28:31], v[52:55]
	v_mfma_f32_16x16x32_bf16 v[48:51], v[80:83], v[32:35], v[48:51]
	v_mfma_f32_16x16x32_bf16 v[52:55], v[80:83], v[36:39], v[52:55]
	v_mfma_f32_16x16x32_bf16 v[48:51], v[88:91], v[40:43], v[48:51]
	v_mfma_f32_16x16x32_bf16 v[52:55], v[88:91], v[44:47], v[52:55]
	ds_read_b128 v[16:19], v63 offset:256
	ds_read_b128 v[20:23], v63 offset:8704
	ds_read_b128 v[24:27], v63 offset:320
	ds_read_b128 v[28:31], v63 offset:8768
	ds_read_b128 v[32:35], v63 offset:384
	ds_read_b128 v[36:39], v63 offset:8832
	ds_read_b128 v[40:43], v63 offset:448
	ds_read_b128 v[44:47], v63 offset:8896
	s_waitcnt lgkmcnt(0)
	v_mfma_f32_16x16x32_bf16 v[48:51], v[96:99], v[16:19], v[48:51]
	v_mfma_f32_16x16x32_bf16 v[52:55], v[96:99], v[20:23], v[52:55]
	v_mfma_f32_16x16x32_bf16 v[48:51], v[104:107], v[24:27], v[48:51]
	v_mfma_f32_16x16x32_bf16 v[52:55], v[104:107], v[28:31], v[52:55]
	v_mfma_f32_16x16x32_bf16 v[48:51], v[112:115], v[32:35], v[48:51]
	v_mfma_f32_16x16x32_bf16 v[52:55], v[112:115], v[36:39], v[52:55]
	v_mfma_f32_16x16x32_bf16 v[48:51], v[120:123], v[40:43], v[48:51]
	v_mfma_f32_16x16x32_bf16 v[52:55], v[120:123], v[44:47], v[52:55]
	s_nop 9
	s_lshr_b32 s58, s22, 3
	s_and_b32 s59, s22, 7
	s_lshr_b32 s60, s25, 4
	s_cmp_lg_u32 s24, 0
	s_cbranch_scc1 .Lpre_E_notq
	s_lshl_b32 s61, s22, 15
	s_lshl_b32 s37, s25, 2
	s_add_u32 s61, s61, s37
	s_add_u32 s62, s16, s61
	s_addc_u32 s63, s17, 0
	v_lshl_or_b32 v60, v2, 10, v14
	global_store_dwordx4 v60, v[48:51], s[62:63]
	s_add_u32 s62, s62, 0x4000
	s_addc_u32 s63, s63, 0
	global_store_dwordx4 v60, v[52:55], s[62:63]
	s_endpgm
.Lpre_E_notq:
	s_cmp_lg_u32 s24, 1
	s_cbranch_scc1 .Lpre_E_v
	s_lshl_b32 s61, s58, 3
	s_add_u32 s61, s61, s59
	s_lshl_b32 s61, s61, 4
	s_add_u32 s61, s61, s60
	s_lshl_b32 s61, s61, 10
	s_add_u32 s62, s18, s61
	s_addc_u32 s63, s19, 0
	v_lshlrev_b32_e32 v60, 10, v62
	v_lshrrev_b32_e32 v61, 1, v3
	v_lshl_or_b32 v60, v61, 9, v60
	v_lshl_or_b32 v60, v2, 4, v60
	v_and_b32_e32 v61, 1, v3
	v_lshl_or_b32 v60, v61, 3, v60
	v_cvt_pk_bf16_f32 v48, v48, v49
	v_cvt_pk_bf16_f32 v49, v50, v51
	v_cvt_pk_bf16_f32 v52, v52, v53
	v_cvt_pk_bf16_f32 v53, v54, v55
	global_store_dwordx2 v60, v[48:49], s[62:63]
	global_store_dwordx2 v60, v[52:53], s[62:63] offset:256
	s_endpgm
.Lpre_E_v:
	s_lshl_b32 s61, s58, 4
	s_add_u32 s61, s61, s60
	s_lshl_b32 s61, s61, 3
	s_add_u32 s61, s61, s59
	s_lshl_b32 s61, s61, 10
	s_add_u32 s62, s20, s61
	s_addc_u32 s63, s21, 0
	v_lshlrev_b32_e32 v60, 13, v62
	v_lshrrev_b32_e32 v61, 3, v2
	v_lshl_or_b32 v60, v61, 8, v60
	v_lshl_or_b32 v60, v3, 6, v60
	v_and_b32_e32 v61, 7, v2
	v_lshl_or_b32 v60, v61, 1, v60
	s_waitcnt vmcnt(0)
	v_add_f32_e32 v48, v48, v56
	v_add_f32_e32 v49, v49, v57
	v_add_f32_e32 v50, v50, v58
	v_add_f32_e32 v51, v51, v59
	v_add_f32_e32 v52, v52, v56
	v_add_f32_e32 v53, v53, v57
	v_add_f32_e32 v54, v54, v58
	v_add_f32_e32 v55, v55, v59
	v_cvt_pk_bf16_f32 v48, v48, v48
	v_cvt_pk_bf16_f32 v49, v49, v49
	v_cvt_pk_bf16_f32 v50, v50, v50
	v_cvt_pk_bf16_f32 v51, v51, v51
	v_cvt_pk_bf16_f32 v52, v52, v52
	v_cvt_pk_bf16_f32 v53, v53, v53
	v_cvt_pk_bf16_f32 v54, v54, v54
	v_cvt_pk_bf16_f32 v55, v55, v55
	global_store_short v60, v48, s[62:63]
	global_store_short v60, v49, s[62:63] offset:16
	global_store_short v60, v50, s[62:63] offset:32
	global_store_short v60, v51, s[62:63] offset:48
	global_store_short v60, v52, s[62:63] offset:512
	global_store_short v60, v53, s[62:63] offset:528
	global_store_short v60, v54, s[62:63] offset:544
	global_store_short v60, v55, s[62:63] offset:560
.Lpre_E_exit:
	s_endpgm
.Lpre_roleA_pre:
	s_load_dwordx2 s[28:29], s[0:1], 0x18
	s_branch .Lpre_orig

.LBB1_5:
	s_andn2_saveexec_b64 s[8:9], s[8:9]
	s_cbranch_execz .LBB1_9
	v_cmp_eq_u32_e32 vcc, 1, v192
	s_and_saveexec_b64 s[10:11], vcc
	s_cbranch_execz .LBB1_8
	s_mov_b64 s[20:21], s[72:73]
	v_add_u32_e32 v22, 0x40000, v176
	v_add_u32_e32 v23, 0x41000, v176
	s_waitcnt lgkmcnt(0)
	global_load_dwordx4 v[24:27], v22, s[20:21]
	global_load_dwordx4 v[28:31], v22, s[20:21] offset:1024
	global_load_dwordx4 v[32:35], v22, s[20:21] offset:2048
	global_load_dwordx4 v[36:39], v22, s[20:21] offset:3072
	global_load_dwordx4 v[40:43], v23, s[20:21]
	global_load_dwordx4 v[44:47], v23, s[20:21] offset:1024
	global_load_dwordx4 v[48:51], v23, s[20:21] offset:2048
	global_load_dwordx4 v[52:55], v23, s[20:21] offset:3072

.LBB1_12:
	s_or_b64 exec, exec, s[12:13]
	v_lshlrev_b32_e32 v174, 12, v192
	v_mov_b32_e32 v175, 0
	v_mul_u32_u24_e32 v1, 0x1200, v192
	v_mov_b32_e32 v177, v175
	v_lshl_add_u64 v[8:9], s[10:11], 0, v[174:175]
	v_lshlrev_b32_e32 v7, 9, v192
	v_lshl_add_u64 v[180:181], v[8:9], 0, v[176:177]
	s_mov_b64 s[0:1], 0xa000
	v_sub_u32_e32 v186, v1, v7
	v_lshl_add_u64 v[8:9], v[180:181], 0, s[0:1]
	v_readfirstlane_b32 s0, v186
	s_mov_b32 m0, s0
	s_mov_b64 s[0:1], 0xe000
	v_add_u32_e32 v190, 0x5000, v186
	global_load_lds_dwordx4 v[8:9], off
	global_load_lds_dwordx4 v[8:9], off offset:1024
	global_load_lds_dwordx4 v[8:9], off offset:2048
	global_load_lds_dwordx4 v[8:9], off offset:3072
	v_lshl_add_u64 v[8:9], v[180:181], 0, s[0:1]
	v_readfirstlane_b32 s0, v190
	s_mov_b32 m0, s0
	s_mov_b64 s[0:1], 0x12000
	v_add_u32_e32 v187, 0xa000, v186
	s_mov_b32 s3, 0
	global_load_lds_dwordx4 v[8:9], off
	global_load_lds_dwordx4 v[8:9], off offset:1024
	global_load_lds_dwordx4 v[8:9], off offset:2048
	global_load_lds_dwordx4 v[8:9], off offset:3072
	v_lshl_add_u64 v[8:9], v[180:181], 0, s[0:1]
	v_readfirstlane_b32 s0, v187
	s_mov_b32 m0, s0
	s_lshl_b64 s[0:1], s[2:3], 8
	s_lshl_b32 s2, s14, 7
	s_or_b32 s0, s0, s2
	v_lshl_or_b32 v182, v192, 5, s0
	v_mov_b32_e32 v183, s1
	v_lshlrev_b64 v[178:179], 9, v[182:183]
	global_load_lds_dwordx4 v[8:9], off
	global_load_lds_dwordx4 v[8:9], off offset:1024
	global_load_lds_dwordx4 v[8:9], off offset:2048
	global_load_lds_dwordx4 v[8:9], off offset:3072
	v_lshl_add_u64 v[8:9], s[8:9], 0, v[178:179]
	v_and_b32_e32 v174, 0x70, v6
	v_lshl_add_u64 v[6:7], v[8:9], 0, v[174:175]
	v_lshlrev_b32_e32 v8, 6, v0
	v_and_b32_e32 v8, 0xe00, v8
	v_mov_b32_e32 v9, v175
	v_or_b32_e32 v12, 0x1000, v8
	v_mov_b32_e32 v13, v175
	v_or_b32_e32 v16, 0x2000, v8
	v_mov_b32_e32 v17, v175
	v_lshl_add_u64 v[10:11], v[6:7], 0, v[8:9]
	v_lshl_add_u64 v[14:15], v[6:7], 0, v[12:13]
	v_lshl_add_u64 v[18:19], v[6:7], 0, v[16:17]
	v_or_b32_e32 v8, 0x3000, v8
	s_mov_b64 s[0:1], 0x80
	global_load_dwordx4 v[134:137], v[14:15], off nt
	global_load_dwordx4 v[130:133], v[18:19], off nt
	v_lshl_add_u64 v[14:15], v[6:7], 0, v[8:9]
	v_lshl_add_u64 v[18:19], v[6:7], 0, s[0:1]
	global_load_dwordx4 v[142:145], v[10:11], off nt
	global_load_dwordx4 v[114:117], v[10:11], off offset:128 nt
	v_lshl_add_u64 v[20:21], v[18:19], 0, v[12:13]
	global_load_dwordx4 v[138:141], v[14:15], off nt
	global_load_dwordx4 v[118:121], v[20:21], off nt
	v_lshl_add_u64 v[14:15], v[18:19], 0, v[16:17]
	s_mov_b64 s[0:1], 0x100
	v_lshl_add_u64 v[18:19], v[18:19], 0, v[8:9]
	global_load_dwordx4 v[122:125], v[14:15], off nt
	global_load_dwordx4 v[126:129], v[18:19], off nt
	v_lshl_add_u64 v[14:15], v[6:7], 0, s[0:1]
	s_mov_b64 s[0:1], 0x180
	v_lshl_add_u64 v[18:19], v[14:15], 0, v[12:13]
	v_lshl_add_u64 v[6:7], v[6:7], 0, s[0:1]
	v_lshl_add_u64 v[20:21], v[14:15], 0, v[16:17]
	global_load_dwordx4 v[94:97], v[18:19], off nt
	global_load_dwordx4 v[98:101], v[20:21], off nt
	v_lshl_add_u64 v[14:15], v[14:15], 0, v[8:9]
	global_load_dwordx4 v[102:105], v[10:11], off offset:256 nt
	global_load_dwordx4 v[66:69], v[10:11], off offset:384 nt
	v_lshl_add_u64 v[10:11], v[6:7], 0, v[12:13]
	global_load_dwordx4 v[106:109], v[14:15], off nt
	global_load_dwordx4 v[70:73], v[10:11], off nt
	v_lshl_add_u64 v[10:11], v[6:7], 0, v[16:17]
	v_lshl_add_u64 v[6:7], v[6:7], 0, v[8:9]
	global_load_dwordx4 v[74:77], v[10:11], off nt
	global_load_dwordx4 v[78:81], v[6:7], off nt
	v_and_b32_e32 v189, 32, v191
	s_waitcnt vmcnt(16)
	v_readfirstlane_b32 s22, v192
	s_cmp_lg_u32 s22, 1
	s_cbranch_scc1 .Ledge_nosum
	v_pk_add_f32 v[24:25], v[24:25], v[28:29]
	v_pk_add_f32 v[26:27], v[26:27], v[30:31]
	v_pk_add_f32 v[32:33], v[32:33], v[36:37]
	v_pk_add_f32 v[34:35], v[34:35], v[38:39]
	v_pk_add_f32 v[40:41], v[40:41], v[44:45]
	v_pk_add_f32 v[42:43], v[42:43], v[46:47]
	v_pk_add_f32 v[48:49], v[48:49], v[52:53]
	v_pk_add_f32 v[50:51], v[50:51], v[54:55]
	v_pk_add_f32 v[24:25], v[24:25], v[32:33]
	v_pk_add_f32 v[26:27], v[26:27], v[34:35]
	v_pk_add_f32 v[40:41], v[40:41], v[48:49]
	v_pk_add_f32 v[42:43], v[42:43], v[50:51]
	v_pk_add_f32 v[24:25], v[24:25], v[40:41]
	v_pk_add_f32 v[26:27], v[26:27], v[42:43]
	ds_write_b128 v176, v[24:27] offset:58368
